# cache-policy hint: nt on the pass-2 score reloads (their last use), stores unchanged; on top of v26
# speedup vs baseline: 1.0011x; 1.0000x over previous
.LBB0_552:
	v_readlane_b32 s100, v254, 38
	v_readlane_b32 s101, v254, 39
	v_mov_b32_e32 v77, v4
	s_mov_b32 s13, 0
	s_nop 2
	s_add_i32 s1, s13, 1
	s_min_u32 s1, s1, s12
	s_lshl_b32 s1, s1, 14
	v_add_u32_e32 v78, s1, v77
	global_load_dwordx2 v[80:81], v78, s[100:101] nt
	global_load_dwordx2 v[82:83], v78, s[100:101] offset:512 nt
	global_load_dwordx2 v[84:85], v78, s[100:101] offset:1024 nt
	global_load_dwordx2 v[86:87], v78, s[100:101] offset:1536 nt
	s_add_i32 s1, s13, 2
	s_min_u32 s1, s1, s12
	s_lshl_b32 s1, s1, 14
	v_add_u32_e32 v78, s1, v77
	global_load_dwordx2 v[88:89], v78, s[100:101] nt
	global_load_dwordx2 v[90:91], v78, s[100:101] offset:512 nt
	global_load_dwordx2 v[92:93], v78, s[100:101] offset:1024 nt
	global_load_dwordx2 v[94:95], v78, s[100:101] offset:1536 nt
.Lp2_loop_a:
	s_add_i32 s1, s13, 3
	s_min_u32 s1, s1, s12
	s_lshl_b32 s1, s1, 14
	v_add_u32_e32 v78, s1, v77
	global_load_dwordx2 v[96:97], v78, s[100:101] nt
	global_load_dwordx2 v[98:99], v78, s[100:101] offset:512 nt
	global_load_dwordx2 v[100:101], v78, s[100:101] offset:1024 nt
	global_load_dwordx2 v[102:103], v78, s[100:101] offset:1536 nt
	v_sub_u32_e32 v74, v44, v23
	s_waitcnt vmcnt(15)
	v_cvt_f32_f16_e32 v24, v18
	v_cvt_f32_f16_sdwa v25, v18 dst_sel:DWORD dst_unused:UNUSED_PAD src0_sel:WORD_1
	v_cvt_f32_f16_e32 v26, v19
	v_cvt_f32_f16_sdwa v27, v19 dst_sel:DWORD dst_unused:UNUSED_PAD src0_sel:WORD_1
	v_add_u32_e32 v73, 0x64, v74
	v_med3_i32 v73, v73, 0, 4
	v_lshlrev_b32_e64 v73, v73, 1
	v_add_u32_e32 v73, -1, v73
	v_cmp_le_f32_e64 s[28:29], v0, v27
	v_cmp_le_f32_e64 s[30:31], v20, v27
	v_cmp_le_f32_e64 s[34:35], v0, v26
	v_cmp_le_f32_e64 s[36:37], v20, v26
	v_addc_co_u32_e64 v28, s[0:1], 0, 0, s[28:29]
	v_addc_co_u32_e64 v72, s[0:1], 0, 0, s[30:31]
	v_cmp_le_f32_e64 s[28:29], v0, v25
	v_cmp_le_f32_e64 s[30:31], v20, v25
	v_addc_co_u32_e64 v28, s[0:1], v28, v28, s[34:35]
	v_addc_co_u32_e64 v72, s[0:1], v72, v72, s[36:37]
	v_cmp_le_f32_e64 s[34:35], v0, v24
	v_cmp_le_f32_e64 s[36:37], v20, v24
	v_addc_co_u32_e64 v28, s[0:1], v28, v28, s[28:29]
	v_addc_co_u32_e64 v72, s[0:1], v72, v72, s[30:31]
	s_nop 1
	v_addc_co_u32_e64 v28, s[0:1], v28, v28, s[34:35]
	v_addc_co_u32_e64 v72, s[0:1], v72, v72, s[36:37]
	v_bfi_b32 v72, v28, 0, v72
	v_and_b32_e32 v28, v28, v73
	v_and_b32_e32 v72, v72, v73
	v_lshl_or_b32 v75, v72, 16, v28
	v_lshlrev_b32_e32 v75, v21, v75
	v_mov_b32_e32 v76, v75
	s_nop 1
	v_permlane16_swap_b32_e32 v75, v76
	v_or_b32_e32 v75, v75, v76
	v_mov_b32_e32 v76, v75
	s_nop 1
	v_permlane32_swap_b32_e32 v75, v76
	s_and_saveexec_b64 s[0:1], vcc
	v_or_b32_e32 v75, v75, v76
	v_add_u32_e32 v76, 0x18000, v22
	ds_write_b16 v76, v75
	ds_write_b16_d16_hi v22, v75 offset:32768
	s_or_b64 exec, exec, s[0:1]
	s_waitcnt vmcnt(14)
	v_cvt_f32_f16_e32 v24, v16
	v_cvt_f32_f16_sdwa v25, v16 dst_sel:DWORD dst_unused:UNUSED_PAD src0_sel:WORD_1
	v_cvt_f32_f16_e32 v26, v17
	v_cvt_f32_f16_sdwa v27, v17 dst_sel:DWORD dst_unused:UNUSED_PAD src0_sel:WORD_1
	v_add_u32_e32 v73, 0x44, v74
	v_med3_i32 v73, v73, 0, 4
	v_lshlrev_b32_e64 v73, v73, 1
	v_add_u32_e32 v73, -1, v73
	v_cmp_le_f32_e64 s[28:29], v0, v27
	v_cmp_le_f32_e64 s[30:31], v20, v27
	v_cmp_le_f32_e64 s[34:35], v0, v26
	v_cmp_le_f32_e64 s[36:37], v20, v26
	v_addc_co_u32_e64 v28, s[0:1], 0, 0, s[28:29]
	v_addc_co_u32_e64 v72, s[0:1], 0, 0, s[30:31]
	v_cmp_le_f32_e64 s[28:29], v0, v25
	v_cmp_le_f32_e64 s[30:31], v20, v25
	v_addc_co_u32_e64 v28, s[0:1], v28, v28, s[34:35]
	v_addc_co_u32_e64 v72, s[0:1], v72, v72, s[36:37]
	v_cmp_le_f32_e64 s[34:35], v0, v24
	v_cmp_le_f32_e64 s[36:37], v20, v24
	v_addc_co_u32_e64 v28, s[0:1], v28, v28, s[28:29]
	v_addc_co_u32_e64 v72, s[0:1], v72, v72, s[30:31]
	s_nop 1
	v_addc_co_u32_e64 v28, s[0:1], v28, v28, s[34:35]
	v_addc_co_u32_e64 v72, s[0:1], v72, v72, s[36:37]
	v_bfi_b32 v72, v28, 0, v72
	v_and_b32_e32 v28, v28, v73
	v_and_b32_e32 v72, v72, v73
	v_lshl_or_b32 v75, v72, 16, v28
	v_lshlrev_b32_e32 v75, v21, v75
	v_mov_b32_e32 v76, v75
	s_nop 1
	v_permlane16_swap_b32_e32 v75, v76
	v_or_b32_e32 v75, v75, v76
	v_mov_b32_e32 v76, v75
	s_nop 1
	v_permlane32_swap_b32_e32 v75, v76
	s_and_saveexec_b64 s[0:1], vcc
	v_or_b32_e32 v75, v75, v76
	v_add_u32_e32 v76, 0x18004, v22
	ds_write_b16 v76, v75
	ds_write_b16_d16_hi v22, v75 offset:32772
	s_or_b64 exec, exec, s[0:1]
	s_waitcnt vmcnt(13)
	v_cvt_f32_f16_e32 v24, v14
	v_cvt_f32_f16_sdwa v25, v14 dst_sel:DWORD dst_unused:UNUSED_PAD src0_sel:WORD_1
	v_cvt_f32_f16_e32 v26, v15
	v_cvt_f32_f16_sdwa v27, v15 dst_sel:DWORD dst_unused:UNUSED_PAD src0_sel:WORD_1
	v_add_u32_e32 v73, 36, v74
	v_med3_i32 v73, v73, 0, 4
	v_lshlrev_b32_e64 v73, v73, 1
	v_add_u32_e32 v73, -1, v73
	v_cmp_le_f32_e64 s[28:29], v0, v27
	v_cmp_le_f32_e64 s[30:31], v20, v27
	v_cmp_le_f32_e64 s[34:35], v0, v26
	v_cmp_le_f32_e64 s[36:37], v20, v26
	v_addc_co_u32_e64 v28, s[0:1], 0, 0, s[28:29]
	v_addc_co_u32_e64 v72, s[0:1], 0, 0, s[30:31]
	v_cmp_le_f32_e64 s[28:29], v0, v25
	v_cmp_le_f32_e64 s[30:31], v20, v25
	v_addc_co_u32_e64 v28, s[0:1], v28, v28, s[34:35]
	v_addc_co_u32_e64 v72, s[0:1], v72, v72, s[36:37]
	v_cmp_le_f32_e64 s[34:35], v0, v24
	v_cmp_le_f32_e64 s[36:37], v20, v24
	v_addc_co_u32_e64 v28, s[0:1], v28, v28, s[28:29]
	v_addc_co_u32_e64 v72, s[0:1], v72, v72, s[30:31]
	s_nop 1
	v_addc_co_u32_e64 v28, s[0:1], v28, v28, s[34:35]
	v_addc_co_u32_e64 v72, s[0:1], v72, v72, s[36:37]
	v_bfi_b32 v72, v28, 0, v72
	v_and_b32_e32 v28, v28, v73
	v_and_b32_e32 v72, v72, v73
	v_lshl_or_b32 v75, v72, 16, v28
	v_lshlrev_b32_e32 v75, v21, v75
	v_mov_b32_e32 v76, v75
	s_nop 1
	v_permlane16_swap_b32_e32 v75, v76
	v_or_b32_e32 v75, v75, v76
	v_mov_b32_e32 v76, v75
	s_nop 1
	v_permlane32_swap_b32_e32 v75, v76
	s_and_saveexec_b64 s[0:1], vcc
	v_or_b32_e32 v75, v75, v76
	v_add_u32_e32 v76, 0x18008, v22
	ds_write_b16 v76, v75
	ds_write_b16_d16_hi v22, v75 offset:32776
	s_or_b64 exec, exec, s[0:1]
	s_waitcnt vmcnt(12)
	v_cvt_f32_f16_e32 v24, v12
	v_cvt_f32_f16_sdwa v25, v12 dst_sel:DWORD dst_unused:UNUSED_PAD src0_sel:WORD_1
	v_cvt_f32_f16_e32 v26, v13
	v_cvt_f32_f16_sdwa v27, v13 dst_sel:DWORD dst_unused:UNUSED_PAD src0_sel:WORD_1
	v_add_u32_e32 v73, 4, v74
	v_med3_i32 v73, v73, 0, 4
	v_lshlrev_b32_e64 v73, v73, 1
	v_add_u32_e32 v73, -1, v73
	v_cmp_le_f32_e64 s[28:29], v0, v27
	v_cmp_le_f32_e64 s[30:31], v20, v27
	v_cmp_le_f32_e64 s[34:35], v0, v26
	v_cmp_le_f32_e64 s[36:37], v20, v26
	v_addc_co_u32_e64 v28, s[0:1], 0, 0, s[28:29]
	v_addc_co_u32_e64 v72, s[0:1], 0, 0, s[30:31]
	v_cmp_le_f32_e64 s[28:29], v0, v25
	v_cmp_le_f32_e64 s[30:31], v20, v25
	v_addc_co_u32_e64 v28, s[0:1], v28, v28, s[34:35]
	v_addc_co_u32_e64 v72, s[0:1], v72, v72, s[36:37]
	v_cmp_le_f32_e64 s[34:35], v0, v24
	v_cmp_le_f32_e64 s[36:37], v20, v24
	v_addc_co_u32_e64 v28, s[0:1], v28, v28, s[28:29]
	v_addc_co_u32_e64 v72, s[0:1], v72, v72, s[30:31]
	s_nop 1
	v_addc_co_u32_e64 v28, s[0:1], v28, v28, s[34:35]
	v_addc_co_u32_e64 v72, s[0:1], v72, v72, s[36:37]
	v_bfi_b32 v72, v28, 0, v72
	v_and_b32_e32 v28, v28, v73
	v_and_b32_e32 v72, v72, v73
	v_lshl_or_b32 v75, v72, 16, v28
	v_lshlrev_b32_e32 v75, v21, v75
	v_mov_b32_e32 v76, v75
	s_nop 1
	v_permlane16_swap_b32_e32 v75, v76
	v_or_b32_e32 v75, v75, v76
	v_mov_b32_e32 v76, v75
	s_nop 1
	v_permlane32_swap_b32_e32 v75, v76
	s_and_saveexec_b64 s[0:1], vcc
	v_or_b32_e32 v75, v75, v76
	v_add_u32_e32 v76, 0x1800c, v22
	ds_write_b16 v76, v75
	ds_write_b16_d16_hi v22, v75 offset:32780
	s_or_b64 exec, exec, s[0:1]
	s_add_i32 s13, s13, 1
	v_add_u32_e32 v22, 16, v22
	v_add_u32_e32 v23, 0x80, v23
	s_cmp_eq_u32 s13, s50
	s_cbranch_scc1 .Lp2_exit_a
	s_add_i32 s1, s13, 3
	s_min_u32 s1, s1, s12
	s_lshl_b32 s1, s1, 14
	v_add_u32_e32 v78, s1, v77
	global_load_dwordx2 v[18:19], v78, s[100:101] nt
	global_load_dwordx2 v[16:17], v78, s[100:101] offset:512 nt
	global_load_dwordx2 v[14:15], v78, s[100:101] offset:1024 nt
	global_load_dwordx2 v[12:13], v78, s[100:101] offset:1536 nt
	v_sub_u32_e32 v74, v44, v23
	s_waitcnt vmcnt(15)
	v_cvt_f32_f16_e32 v24, v80
	v_cvt_f32_f16_sdwa v25, v80 dst_sel:DWORD dst_unused:UNUSED_PAD src0_sel:WORD_1
	v_cvt_f32_f16_e32 v26, v81
	v_cvt_f32_f16_sdwa v27, v81 dst_sel:DWORD dst_unused:UNUSED_PAD src0_sel:WORD_1
	v_add_u32_e32 v73, 0x64, v74
	v_med3_i32 v73, v73, 0, 4
	v_lshlrev_b32_e64 v73, v73, 1
	v_add_u32_e32 v73, -1, v73
	v_cmp_le_f32_e64 s[28:29], v0, v27
	v_cmp_le_f32_e64 s[30:31], v20, v27
	v_cmp_le_f32_e64 s[34:35], v0, v26
	v_cmp_le_f32_e64 s[36:37], v20, v26
	v_addc_co_u32_e64 v28, s[0:1], 0, 0, s[28:29]
	v_addc_co_u32_e64 v72, s[0:1], 0, 0, s[30:31]
	v_cmp_le_f32_e64 s[28:29], v0, v25
	v_cmp_le_f32_e64 s[30:31], v20, v25
	v_addc_co_u32_e64 v28, s[0:1], v28, v28, s[34:35]
	v_addc_co_u32_e64 v72, s[0:1], v72, v72, s[36:37]
	v_cmp_le_f32_e64 s[34:35], v0, v24
	v_cmp_le_f32_e64 s[36:37], v20, v24
	v_addc_co_u32_e64 v28, s[0:1], v28, v28, s[28:29]
	v_addc_co_u32_e64 v72, s[0:1], v72, v72, s[30:31]
	s_nop 1
	v_addc_co_u32_e64 v28, s[0:1], v28, v28, s[34:35]
	v_addc_co_u32_e64 v72, s[0:1], v72, v72, s[36:37]
	v_bfi_b32 v72, v28, 0, v72
	v_and_b32_e32 v28, v28, v73
	v_and_b32_e32 v72, v72, v73
	v_lshl_or_b32 v75, v72, 16, v28
	v_lshlrev_b32_e32 v75, v21, v75
	v_mov_b32_e32 v76, v75
	s_nop 1
	v_permlane16_swap_b32_e32 v75, v76
	v_or_b32_e32 v75, v75, v76
	v_mov_b32_e32 v76, v75
	s_nop 1
	v_permlane32_swap_b32_e32 v75, v76
	s_and_saveexec_b64 s[0:1], vcc
	v_or_b32_e32 v75, v75, v76
	v_add_u32_e32 v76, 0x18000, v22
	ds_write_b16 v76, v75
	ds_write_b16_d16_hi v22, v75 offset:32768
	s_or_b64 exec, exec, s[0:1]
	s_waitcnt vmcnt(14)
	v_cvt_f32_f16_e32 v24, v82
	v_cvt_f32_f16_sdwa v25, v82 dst_sel:DWORD dst_unused:UNUSED_PAD src0_sel:WORD_1
	v_cvt_f32_f16_e32 v26, v83
	v_cvt_f32_f16_sdwa v27, v83 dst_sel:DWORD dst_unused:UNUSED_PAD src0_sel:WORD_1
	v_add_u32_e32 v73, 0x44, v74
	v_med3_i32 v73, v73, 0, 4
	v_lshlrev_b32_e64 v73, v73, 1
	v_add_u32_e32 v73, -1, v73
	v_cmp_le_f32_e64 s[28:29], v0, v27
	v_cmp_le_f32_e64 s[30:31], v20, v27
	v_cmp_le_f32_e64 s[34:35], v0, v26
	v_cmp_le_f32_e64 s[36:37], v20, v26
	v_addc_co_u32_e64 v28, s[0:1], 0, 0, s[28:29]
	v_addc_co_u32_e64 v72, s[0:1], 0, 0, s[30:31]
	v_cmp_le_f32_e64 s[28:29], v0, v25
	v_cmp_le_f32_e64 s[30:31], v20, v25
	v_addc_co_u32_e64 v28, s[0:1], v28, v28, s[34:35]
	v_addc_co_u32_e64 v72, s[0:1], v72, v72, s[36:37]
	v_cmp_le_f32_e64 s[34:35], v0, v24
	v_cmp_le_f32_e64 s[36:37], v20, v24
	v_addc_co_u32_e64 v28, s[0:1], v28, v28, s[28:29]
	v_addc_co_u32_e64 v72, s[0:1], v72, v72, s[30:31]
	s_nop 1
	v_addc_co_u32_e64 v28, s[0:1], v28, v28, s[34:35]
	v_addc_co_u32_e64 v72, s[0:1], v72, v72, s[36:37]
	v_bfi_b32 v72, v28, 0, v72
	v_and_b32_e32 v28, v28, v73
	v_and_b32_e32 v72, v72, v73
	v_lshl_or_b32 v75, v72, 16, v28
	v_lshlrev_b32_e32 v75, v21, v75
	v_mov_b32_e32 v76, v75
	s_nop 1
	v_permlane16_swap_b32_e32 v75, v76
	v_or_b32_e32 v75, v75, v76
	v_mov_b32_e32 v76, v75
	s_nop 1
	v_permlane32_swap_b32_e32 v75, v76
	s_and_saveexec_b64 s[0:1], vcc
	v_or_b32_e32 v75, v75, v76
	v_add_u32_e32 v76, 0x18004, v22
	ds_write_b16 v76, v75
	ds_write_b16_d16_hi v22, v75 offset:32772
	s_or_b64 exec, exec, s[0:1]
	s_waitcnt vmcnt(13)
	v_cvt_f32_f16_e32 v24, v84
	v_cvt_f32_f16_sdwa v25, v84 dst_sel:DWORD dst_unused:UNUSED_PAD src0_sel:WORD_1
	v_cvt_f32_f16_e32 v26, v85
	v_cvt_f32_f16_sdwa v27, v85 dst_sel:DWORD dst_unused:UNUSED_PAD src0_sel:WORD_1
	v_add_u32_e32 v73, 36, v74
	v_med3_i32 v73, v73, 0, 4
	v_lshlrev_b32_e64 v73, v73, 1
	v_add_u32_e32 v73, -1, v73
	v_cmp_le_f32_e64 s[28:29], v0, v27
	v_cmp_le_f32_e64 s[30:31], v20, v27
	v_cmp_le_f32_e64 s[34:35], v0, v26
	v_cmp_le_f32_e64 s[36:37], v20, v26
	v_addc_co_u32_e64 v28, s[0:1], 0, 0, s[28:29]
	v_addc_co_u32_e64 v72, s[0:1], 0, 0, s[30:31]
	v_cmp_le_f32_e64 s[28:29], v0, v25
	v_cmp_le_f32_e64 s[30:31], v20, v25
	v_addc_co_u32_e64 v28, s[0:1], v28, v28, s[34:35]
	v_addc_co_u32_e64 v72, s[0:1], v72, v72, s[36:37]
	v_cmp_le_f32_e64 s[34:35], v0, v24
	v_cmp_le_f32_e64 s[36:37], v20, v24
	v_addc_co_u32_e64 v28, s[0:1], v28, v28, s[28:29]
	v_addc_co_u32_e64 v72, s[0:1], v72, v72, s[30:31]
	s_nop 1
	v_addc_co_u32_e64 v28, s[0:1], v28, v28, s[34:35]
	v_addc_co_u32_e64 v72, s[0:1], v72, v72, s[36:37]
	v_bfi_b32 v72, v28, 0, v72
	v_and_b32_e32 v28, v28, v73
	v_and_b32_e32 v72, v72, v73
	v_lshl_or_b32 v75, v72, 16, v28
	v_lshlrev_b32_e32 v75, v21, v75
	v_mov_b32_e32 v76, v75
	s_nop 1
	v_permlane16_swap_b32_e32 v75, v76
	v_or_b32_e32 v75, v75, v76
	v_mov_b32_e32 v76, v75
	s_nop 1
	v_permlane32_swap_b32_e32 v75, v76
	s_and_saveexec_b64 s[0:1], vcc
	v_or_b32_e32 v75, v75, v76
	v_add_u32_e32 v76, 0x18008, v22
	ds_write_b16 v76, v75
	ds_write_b16_d16_hi v22, v75 offset:32776
	s_or_b64 exec, exec, s[0:1]
	s_waitcnt vmcnt(12)
	v_cvt_f32_f16_e32 v24, v86
	v_cvt_f32_f16_sdwa v25, v86 dst_sel:DWORD dst_unused:UNUSED_PAD src0_sel:WORD_1
	v_cvt_f32_f16_e32 v26, v87
	v_cvt_f32_f16_sdwa v27, v87 dst_sel:DWORD dst_unused:UNUSED_PAD src0_sel:WORD_1
	v_add_u32_e32 v73, 4, v74
	v_med3_i32 v73, v73, 0, 4
	v_lshlrev_b32_e64 v73, v73, 1
	v_add_u32_e32 v73, -1, v73
	v_cmp_le_f32_e64 s[28:29], v0, v27
	v_cmp_le_f32_e64 s[30:31], v20, v27
	v_cmp_le_f32_e64 s[34:35], v0, v26
	v_cmp_le_f32_e64 s[36:37], v20, v26
	v_addc_co_u32_e64 v28, s[0:1], 0, 0, s[28:29]
	v_addc_co_u32_e64 v72, s[0:1], 0, 0, s[30:31]
	v_cmp_le_f32_e64 s[28:29], v0, v25
	v_cmp_le_f32_e64 s[30:31], v20, v25
	v_addc_co_u32_e64 v28, s[0:1], v28, v28, s[34:35]
	v_addc_co_u32_e64 v72, s[0:1], v72, v72, s[36:37]
	v_cmp_le_f32_e64 s[34:35], v0, v24
	v_cmp_le_f32_e64 s[36:37], v20, v24
	v_addc_co_u32_e64 v28, s[0:1], v28, v28, s[28:29]
	v_addc_co_u32_e64 v72, s[0:1], v72, v72, s[30:31]
	s_nop 1
	v_addc_co_u32_e64 v28, s[0:1], v28, v28, s[34:35]
	v_addc_co_u32_e64 v72, s[0:1], v72, v72, s[36:37]
	v_bfi_b32 v72, v28, 0, v72
	v_and_b32_e32 v28, v28, v73
	v_and_b32_e32 v72, v72, v73
	v_lshl_or_b32 v75, v72, 16, v28
	v_lshlrev_b32_e32 v75, v21, v75
	v_mov_b32_e32 v76, v75
	s_nop 1
	v_permlane16_swap_b32_e32 v75, v76
	v_or_b32_e32 v75, v75, v76
	v_mov_b32_e32 v76, v75
	s_nop 1
	v_permlane32_swap_b32_e32 v75, v76
	s_and_saveexec_b64 s[0:1], vcc
	v_or_b32_e32 v75, v75, v76
	v_add_u32_e32 v76, 0x1800c, v22
	ds_write_b16 v76, v75
	ds_write_b16_d16_hi v22, v75 offset:32780
	s_or_b64 exec, exec, s[0:1]
	s_add_i32 s13, s13, 1
	v_add_u32_e32 v22, 16, v22
	v_add_u32_e32 v23, 0x80, v23
	s_cmp_eq_u32 s13, s50
	s_cbranch_scc1 .Lp2_exit_a
	s_add_i32 s1, s13, 3
	s_min_u32 s1, s1, s12
	s_lshl_b32 s1, s1, 14
	v_add_u32_e32 v78, s1, v77
	global_load_dwordx2 v[80:81], v78, s[100:101] nt
	global_load_dwordx2 v[82:83], v78, s[100:101] offset:512 nt
	global_load_dwordx2 v[84:85], v78, s[100:101] offset:1024 nt
	global_load_dwordx2 v[86:87], v78, s[100:101] offset:1536 nt
	v_sub_u32_e32 v74, v44, v23
	s_waitcnt vmcnt(15)
	v_cvt_f32_f16_e32 v24, v88
	v_cvt_f32_f16_sdwa v25, v88 dst_sel:DWORD dst_unused:UNUSED_PAD src0_sel:WORD_1
	v_cvt_f32_f16_e32 v26, v89
	v_cvt_f32_f16_sdwa v27, v89 dst_sel:DWORD dst_unused:UNUSED_PAD src0_sel:WORD_1
	v_add_u32_e32 v73, 0x64, v74
	v_med3_i32 v73, v73, 0, 4
	v_lshlrev_b32_e64 v73, v73, 1
	v_add_u32_e32 v73, -1, v73
	v_cmp_le_f32_e64 s[28:29], v0, v27
	v_cmp_le_f32_e64 s[30:31], v20, v27
	v_cmp_le_f32_e64 s[34:35], v0, v26
	v_cmp_le_f32_e64 s[36:37], v20, v26
	v_addc_co_u32_e64 v28, s[0:1], 0, 0, s[28:29]
	v_addc_co_u32_e64 v72, s[0:1], 0, 0, s[30:31]
	v_cmp_le_f32_e64 s[28:29], v0, v25
	v_cmp_le_f32_e64 s[30:31], v20, v25
	v_addc_co_u32_e64 v28, s[0:1], v28, v28, s[34:35]
	v_addc_co_u32_e64 v72, s[0:1], v72, v72, s[36:37]
	v_cmp_le_f32_e64 s[34:35], v0, v24
	v_cmp_le_f32_e64 s[36:37], v20, v24
	v_addc_co_u32_e64 v28, s[0:1], v28, v28, s[28:29]
	v_addc_co_u32_e64 v72, s[0:1], v72, v72, s[30:31]
	s_nop 1
	v_addc_co_u32_e64 v28, s[0:1], v28, v28, s[34:35]
	v_addc_co_u32_e64 v72, s[0:1], v72, v72, s[36:37]
	v_bfi_b32 v72, v28, 0, v72
	v_and_b32_e32 v28, v28, v73
	v_and_b32_e32 v72, v72, v73
	v_lshl_or_b32 v75, v72, 16, v28
	v_lshlrev_b32_e32 v75, v21, v75
	v_mov_b32_e32 v76, v75
	s_nop 1
	v_permlane16_swap_b32_e32 v75, v76
	v_or_b32_e32 v75, v75, v76
	v_mov_b32_e32 v76, v75
	s_nop 1
	v_permlane32_swap_b32_e32 v75, v76
	s_and_saveexec_b64 s[0:1], vcc
	v_or_b32_e32 v75, v75, v76
	v_add_u32_e32 v76, 0x18000, v22
	ds_write_b16 v76, v75
	ds_write_b16_d16_hi v22, v75 offset:32768
	s_or_b64 exec, exec, s[0:1]
	s_waitcnt vmcnt(14)
	v_cvt_f32_f16_e32 v24, v90
	v_cvt_f32_f16_sdwa v25, v90 dst_sel:DWORD dst_unused:UNUSED_PAD src0_sel:WORD_1
	v_cvt_f32_f16_e32 v26, v91
	v_cvt_f32_f16_sdwa v27, v91 dst_sel:DWORD dst_unused:UNUSED_PAD src0_sel:WORD_1
	v_add_u32_e32 v73, 0x44, v74
	v_med3_i32 v73, v73, 0, 4
	v_lshlrev_b32_e64 v73, v73, 1
	v_add_u32_e32 v73, -1, v73
	v_cmp_le_f32_e64 s[28:29], v0, v27
	v_cmp_le_f32_e64 s[30:31], v20, v27
	v_cmp_le_f32_e64 s[34:35], v0, v26
	v_cmp_le_f32_e64 s[36:37], v20, v26
	v_addc_co_u32_e64 v28, s[0:1], 0, 0, s[28:29]
	v_addc_co_u32_e64 v72, s[0:1], 0, 0, s[30:31]
	v_cmp_le_f32_e64 s[28:29], v0, v25
	v_cmp_le_f32_e64 s[30:31], v20, v25
	v_addc_co_u32_e64 v28, s[0:1], v28, v28, s[34:35]
	v_addc_co_u32_e64 v72, s[0:1], v72, v72, s[36:37]
	v_cmp_le_f32_e64 s[34:35], v0, v24
	v_cmp_le_f32_e64 s[36:37], v20, v24
	v_addc_co_u32_e64 v28, s[0:1], v28, v28, s[28:29]
	v_addc_co_u32_e64 v72, s[0:1], v72, v72, s[30:31]
	s_nop 1
	v_addc_co_u32_e64 v28, s[0:1], v28, v28, s[34:35]
	v_addc_co_u32_e64 v72, s[0:1], v72, v72, s[36:37]
	v_bfi_b32 v72, v28, 0, v72
	v_and_b32_e32 v28, v28, v73
	v_and_b32_e32 v72, v72, v73
	v_lshl_or_b32 v75, v72, 16, v28
	v_lshlrev_b32_e32 v75, v21, v75
	v_mov_b32_e32 v76, v75
	s_nop 1
	v_permlane16_swap_b32_e32 v75, v76
	v_or_b32_e32 v75, v75, v76
	v_mov_b32_e32 v76, v75
	s_nop 1
	v_permlane32_swap_b32_e32 v75, v76
	s_and_saveexec_b64 s[0:1], vcc
	v_or_b32_e32 v75, v75, v76
	v_add_u32_e32 v76, 0x18004, v22
	ds_write_b16 v76, v75
	ds_write_b16_d16_hi v22, v75 offset:32772
	s_or_b64 exec, exec, s[0:1]
	s_waitcnt vmcnt(13)
	v_cvt_f32_f16_e32 v24, v92
	v_cvt_f32_f16_sdwa v25, v92 dst_sel:DWORD dst_unused:UNUSED_PAD src0_sel:WORD_1
	v_cvt_f32_f16_e32 v26, v93
	v_cvt_f32_f16_sdwa v27, v93 dst_sel:DWORD dst_unused:UNUSED_PAD src0_sel:WORD_1
	v_add_u32_e32 v73, 36, v74
	v_med3_i32 v73, v73, 0, 4
	v_lshlrev_b32_e64 v73, v73, 1
	v_add_u32_e32 v73, -1, v73
	v_cmp_le_f32_e64 s[28:29], v0, v27
	v_cmp_le_f32_e64 s[30:31], v20, v27
	v_cmp_le_f32_e64 s[34:35], v0, v26
	v_cmp_le_f32_e64 s[36:37], v20, v26
	v_addc_co_u32_e64 v28, s[0:1], 0, 0, s[28:29]
	v_addc_co_u32_e64 v72, s[0:1], 0, 0, s[30:31]
	v_cmp_le_f32_e64 s[28:29], v0, v25
	v_cmp_le_f32_e64 s[30:31], v20, v25
	v_addc_co_u32_e64 v28, s[0:1], v28, v28, s[34:35]
	v_addc_co_u32_e64 v72, s[0:1], v72, v72, s[36:37]
	v_cmp_le_f32_e64 s[34:35], v0, v24
	v_cmp_le_f32_e64 s[36:37], v20, v24
	v_addc_co_u32_e64 v28, s[0:1], v28, v28, s[28:29]
	v_addc_co_u32_e64 v72, s[0:1], v72, v72, s[30:31]
	s_nop 1
	v_addc_co_u32_e64 v28, s[0:1], v28, v28, s[34:35]
	v_addc_co_u32_e64 v72, s[0:1], v72, v72, s[36:37]
	v_bfi_b32 v72, v28, 0, v72
	v_and_b32_e32 v28, v28, v73
	v_and_b32_e32 v72, v72, v73
	v_lshl_or_b32 v75, v72, 16, v28
	v_lshlrev_b32_e32 v75, v21, v75
	v_mov_b32_e32 v76, v75
	s_nop 1
	v_permlane16_swap_b32_e32 v75, v76
	v_or_b32_e32 v75, v75, v76
	v_mov_b32_e32 v76, v75
	s_nop 1
	v_permlane32_swap_b32_e32 v75, v76
	s_and_saveexec_b64 s[0:1], vcc
	v_or_b32_e32 v75, v75, v76
	v_add_u32_e32 v76, 0x18008, v22
	ds_write_b16 v76, v75
	ds_write_b16_d16_hi v22, v75 offset:32776
	s_or_b64 exec, exec, s[0:1]
	s_waitcnt vmcnt(12)
	v_cvt_f32_f16_e32 v24, v94
	v_cvt_f32_f16_sdwa v25, v94 dst_sel:DWORD dst_unused:UNUSED_PAD src0_sel:WORD_1
	v_cvt_f32_f16_e32 v26, v95
	v_cvt_f32_f16_sdwa v27, v95 dst_sel:DWORD dst_unused:UNUSED_PAD src0_sel:WORD_1
	v_add_u32_e32 v73, 4, v74
	v_med3_i32 v73, v73, 0, 4
	v_lshlrev_b32_e64 v73, v73, 1
	v_add_u32_e32 v73, -1, v73
	v_cmp_le_f32_e64 s[28:29], v0, v27
	v_cmp_le_f32_e64 s[30:31], v20, v27
	v_cmp_le_f32_e64 s[34:35], v0, v26
	v_cmp_le_f32_e64 s[36:37], v20, v26
	v_addc_co_u32_e64 v28, s[0:1], 0, 0, s[28:29]
	v_addc_co_u32_e64 v72, s[0:1], 0, 0, s[30:31]
	v_cmp_le_f32_e64 s[28:29], v0, v25
	v_cmp_le_f32_e64 s[30:31], v20, v25
	v_addc_co_u32_e64 v28, s[0:1], v28, v28, s[34:35]
	v_addc_co_u32_e64 v72, s[0:1], v72, v72, s[36:37]
	v_cmp_le_f32_e64 s[34:35], v0, v24
	v_cmp_le_f32_e64 s[36:37], v20, v24
	v_addc_co_u32_e64 v28, s[0:1], v28, v28, s[28:29]
	v_addc_co_u32_e64 v72, s[0:1], v72, v72, s[30:31]
	s_nop 1
	v_addc_co_u32_e64 v28, s[0:1], v28, v28, s[34:35]
	v_addc_co_u32_e64 v72, s[0:1], v72, v72, s[36:37]
	v_bfi_b32 v72, v28, 0, v72
	v_and_b32_e32 v28, v28, v73
	v_and_b32_e32 v72, v72, v73
	v_lshl_or_b32 v75, v72, 16, v28
	v_lshlrev_b32_e32 v75, v21, v75
	v_mov_b32_e32 v76, v75
	s_nop 1
	v_permlane16_swap_b32_e32 v75, v76
	v_or_b32_e32 v75, v75, v76
	v_mov_b32_e32 v76, v75
	s_nop 1
	v_permlane32_swap_b32_e32 v75, v76
	s_and_saveexec_b64 s[0:1], vcc
	v_or_b32_e32 v75, v75, v76
	v_add_u32_e32 v76, 0x1800c, v22
	ds_write_b16 v76, v75
	ds_write_b16_d16_hi v22, v75 offset:32780
	s_or_b64 exec, exec, s[0:1]
	s_add_i32 s13, s13, 1
	v_add_u32_e32 v22, 16, v22
	v_add_u32_e32 v23, 0x80, v23
	s_cmp_eq_u32 s13, s50
	s_cbranch_scc1 .Lp2_exit_a
	s_add_i32 s1, s13, 3
	s_min_u32 s1, s1, s12
	s_lshl_b32 s1, s1, 14
	v_add_u32_e32 v78, s1, v77
	global_load_dwordx2 v[88:89], v78, s[100:101] nt
	global_load_dwordx2 v[90:91], v78, s[100:101] offset:512 nt
	global_load_dwordx2 v[92:93], v78, s[100:101] offset:1024 nt
	global_load_dwordx2 v[94:95], v78, s[100:101] offset:1536 nt
	v_sub_u32_e32 v74, v44, v23
	s_waitcnt vmcnt(15)
	v_cvt_f32_f16_e32 v24, v96
	v_cvt_f32_f16_sdwa v25, v96 dst_sel:DWORD dst_unused:UNUSED_PAD src0_sel:WORD_1
	v_cvt_f32_f16_e32 v26, v97
	v_cvt_f32_f16_sdwa v27, v97 dst_sel:DWORD dst_unused:UNUSED_PAD src0_sel:WORD_1
	v_add_u32_e32 v73, 0x64, v74
	v_med3_i32 v73, v73, 0, 4
	v_lshlrev_b32_e64 v73, v73, 1
	v_add_u32_e32 v73, -1, v73
	v_cmp_le_f32_e64 s[28:29], v0, v27
	v_cmp_le_f32_e64 s[30:31], v20, v27
	v_cmp_le_f32_e64 s[34:35], v0, v26
	v_cmp_le_f32_e64 s[36:37], v20, v26
	v_addc_co_u32_e64 v28, s[0:1], 0, 0, s[28:29]
	v_addc_co_u32_e64 v72, s[0:1], 0, 0, s[30:31]
	v_cmp_le_f32_e64 s[28:29], v0, v25
	v_cmp_le_f32_e64 s[30:31], v20, v25
	v_addc_co_u32_e64 v28, s[0:1], v28, v28, s[34:35]
	v_addc_co_u32_e64 v72, s[0:1], v72, v72, s[36:37]
	v_cmp_le_f32_e64 s[34:35], v0, v24
	v_cmp_le_f32_e64 s[36:37], v20, v24
	v_addc_co_u32_e64 v28, s[0:1], v28, v28, s[28:29]
	v_addc_co_u32_e64 v72, s[0:1], v72, v72, s[30:31]
	s_nop 1
	v_addc_co_u32_e64 v28, s[0:1], v28, v28, s[34:35]
	v_addc_co_u32_e64 v72, s[0:1], v72, v72, s[36:37]
	v_bfi_b32 v72, v28, 0, v72
	v_and_b32_e32 v28, v28, v73
	v_and_b32_e32 v72, v72, v73
	v_lshl_or_b32 v75, v72, 16, v28
	v_lshlrev_b32_e32 v75, v21, v75
	v_mov_b32_e32 v76, v75
	s_nop 1
	v_permlane16_swap_b32_e32 v75, v76
	v_or_b32_e32 v75, v75, v76
	v_mov_b32_e32 v76, v75
	s_nop 1
	v_permlane32_swap_b32_e32 v75, v76
	s_and_saveexec_b64 s[0:1], vcc
	v_or_b32_e32 v75, v75, v76
	v_add_u32_e32 v76, 0x18000, v22
	ds_write_b16 v76, v75
	ds_write_b16_d16_hi v22, v75 offset:32768
	s_or_b64 exec, exec, s[0:1]
	s_waitcnt vmcnt(14)
	v_cvt_f32_f16_e32 v24, v98
	v_cvt_f32_f16_sdwa v25, v98 dst_sel:DWORD dst_unused:UNUSED_PAD src0_sel:WORD_1
	v_cvt_f32_f16_e32 v26, v99
	v_cvt_f32_f16_sdwa v27, v99 dst_sel:DWORD dst_unused:UNUSED_PAD src0_sel:WORD_1
	v_add_u32_e32 v73, 0x44, v74
	v_med3_i32 v73, v73, 0, 4
	v_lshlrev_b32_e64 v73, v73, 1
	v_add_u32_e32 v73, -1, v73
	v_cmp_le_f32_e64 s[28:29], v0, v27
	v_cmp_le_f32_e64 s[30:31], v20, v27
	v_cmp_le_f32_e64 s[34:35], v0, v26
	v_cmp_le_f32_e64 s[36:37], v20, v26
	v_addc_co_u32_e64 v28, s[0:1], 0, 0, s[28:29]
	v_addc_co_u32_e64 v72, s[0:1], 0, 0, s[30:31]
	v_cmp_le_f32_e64 s[28:29], v0, v25
	v_cmp_le_f32_e64 s[30:31], v20, v25
	v_addc_co_u32_e64 v28, s[0:1], v28, v28, s[34:35]
	v_addc_co_u32_e64 v72, s[0:1], v72, v72, s[36:37]
	v_cmp_le_f32_e64 s[34:35], v0, v24
	v_cmp_le_f32_e64 s[36:37], v20, v24
	v_addc_co_u32_e64 v28, s[0:1], v28, v28, s[28:29]
	v_addc_co_u32_e64 v72, s[0:1], v72, v72, s[30:31]
	s_nop 1
	v_addc_co_u32_e64 v28, s[0:1], v28, v28, s[34:35]
	v_addc_co_u32_e64 v72, s[0:1], v72, v72, s[36:37]
	v_bfi_b32 v72, v28, 0, v72
	v_and_b32_e32 v28, v28, v73
	v_and_b32_e32 v72, v72, v73
	v_lshl_or_b32 v75, v72, 16, v28
	v_lshlrev_b32_e32 v75, v21, v75
	v_mov_b32_e32 v76, v75
	s_nop 1
	v_permlane16_swap_b32_e32 v75, v76
	v_or_b32_e32 v75, v75, v76
	v_mov_b32_e32 v76, v75
	s_nop 1
	v_permlane32_swap_b32_e32 v75, v76
	s_and_saveexec_b64 s[0:1], vcc
	v_or_b32_e32 v75, v75, v76
	v_add_u32_e32 v76, 0x18004, v22
	ds_write_b16 v76, v75
	ds_write_b16_d16_hi v22, v75 offset:32772
	s_or_b64 exec, exec, s[0:1]
	s_waitcnt vmcnt(13)
	v_cvt_f32_f16_e32 v24, v100
	v_cvt_f32_f16_sdwa v25, v100 dst_sel:DWORD dst_unused:UNUSED_PAD src0_sel:WORD_1
	v_cvt_f32_f16_e32 v26, v101
	v_cvt_f32_f16_sdwa v27, v101 dst_sel:DWORD dst_unused:UNUSED_PAD src0_sel:WORD_1
	v_add_u32_e32 v73, 36, v74
	v_med3_i32 v73, v73, 0, 4
	v_lshlrev_b32_e64 v73, v73, 1
	v_add_u32_e32 v73, -1, v73
	v_cmp_le_f32_e64 s[28:29], v0, v27
	v_cmp_le_f32_e64 s[30:31], v20, v27
	v_cmp_le_f32_e64 s[34:35], v0, v26
	v_cmp_le_f32_e64 s[36:37], v20, v26
	v_addc_co_u32_e64 v28, s[0:1], 0, 0, s[28:29]
	v_addc_co_u32_e64 v72, s[0:1], 0, 0, s[30:31]
	v_cmp_le_f32_e64 s[28:29], v0, v25
	v_cmp_le_f32_e64 s[30:31], v20, v25
	v_addc_co_u32_e64 v28, s[0:1], v28, v28, s[34:35]
	v_addc_co_u32_e64 v72, s[0:1], v72, v72, s[36:37]
	v_cmp_le_f32_e64 s[34:35], v0, v24
	v_cmp_le_f32_e64 s[36:37], v20, v24
	v_addc_co_u32_e64 v28, s[0:1], v28, v28, s[28:29]
	v_addc_co_u32_e64 v72, s[0:1], v72, v72, s[30:31]
	s_nop 1
	v_addc_co_u32_e64 v28, s[0:1], v28, v28, s[34:35]
	v_addc_co_u32_e64 v72, s[0:1], v72, v72, s[36:37]
	v_bfi_b32 v72, v28, 0, v72
	v_and_b32_e32 v28, v28, v73
	v_and_b32_e32 v72, v72, v73
	v_lshl_or_b32 v75, v72, 16, v28
	v_lshlrev_b32_e32 v75, v21, v75
	v_mov_b32_e32 v76, v75
	s_nop 1
	v_permlane16_swap_b32_e32 v75, v76
	v_or_b32_e32 v75, v75, v76
	v_mov_b32_e32 v76, v75
	s_nop 1
	v_permlane32_swap_b32_e32 v75, v76
	s_and_saveexec_b64 s[0:1], vcc
	v_or_b32_e32 v75, v75, v76
	v_add_u32_e32 v76, 0x18008, v22
	ds_write_b16 v76, v75
	ds_write_b16_d16_hi v22, v75 offset:32776
	s_or_b64 exec, exec, s[0:1]
	s_waitcnt vmcnt(12)
	v_cvt_f32_f16_e32 v24, v102
	v_cvt_f32_f16_sdwa v25, v102 dst_sel:DWORD dst_unused:UNUSED_PAD src0_sel:WORD_1
	v_cvt_f32_f16_e32 v26, v103
	v_cvt_f32_f16_sdwa v27, v103 dst_sel:DWORD dst_unused:UNUSED_PAD src0_sel:WORD_1
	v_add_u32_e32 v73, 4, v74
	v_med3_i32 v73, v73, 0, 4
	v_lshlrev_b32_e64 v73, v73, 1
	v_add_u32_e32 v73, -1, v73
	v_cmp_le_f32_e64 s[28:29], v0, v27
	v_cmp_le_f32_e64 s[30:31], v20, v27
	v_cmp_le_f32_e64 s[34:35], v0, v26
	v_cmp_le_f32_e64 s[36:37], v20, v26
	v_addc_co_u32_e64 v28, s[0:1], 0, 0, s[28:29]
	v_addc_co_u32_e64 v72, s[0:1], 0, 0, s[30:31]
	v_cmp_le_f32_e64 s[28:29], v0, v25
	v_cmp_le_f32_e64 s[30:31], v20, v25
	v_addc_co_u32_e64 v28, s[0:1], v28, v28, s[34:35]
	v_addc_co_u32_e64 v72, s[0:1], v72, v72, s[36:37]
	v_cmp_le_f32_e64 s[34:35], v0, v24
	v_cmp_le_f32_e64 s[36:37], v20, v24
	v_addc_co_u32_e64 v28, s[0:1], v28, v28, s[28:29]
	v_addc_co_u32_e64 v72, s[0:1], v72, v72, s[30:31]
	s_nop 1
	v_addc_co_u32_e64 v28, s[0:1], v28, v28, s[34:35]
	v_addc_co_u32_e64 v72, s[0:1], v72, v72, s[36:37]
	v_bfi_b32 v72, v28, 0, v72
	v_and_b32_e32 v28, v28, v73
	v_and_b32_e32 v72, v72, v73
	v_lshl_or_b32 v75, v72, 16, v28
	v_lshlrev_b32_e32 v75, v21, v75
	v_mov_b32_e32 v76, v75
	s_nop 1
	v_permlane16_swap_b32_e32 v75, v76
	v_or_b32_e32 v75, v75, v76
	v_mov_b32_e32 v76, v75
	s_nop 1
	v_permlane32_swap_b32_e32 v75, v76
	s_and_saveexec_b64 s[0:1], vcc
	v_or_b32_e32 v75, v75, v76
	v_add_u32_e32 v76, 0x1800c, v22
	ds_write_b16 v76, v75
	ds_write_b16_d16_hi v22, v75 offset:32780
	s_or_b64 exec, exec, s[0:1]
	s_add_i32 s13, s13, 1
	v_add_u32_e32 v22, 16, v22
	v_add_u32_e32 v23, 0x80, v23
	s_cmp_eq_u32 s13, s50
	s_cbranch_scc1 .Lp2_exit_a
	s_branch .Lp2_loop_a
